# wave all-reduce sums via DPP + permlane16/32 swaps instead of six serialized ds_bpermute hops (P1, P4, P8, P12), on top of v23
# speedup vs baseline: 1.0132x; 1.0132x over previous
; #define GAS __attribute__((address_space(1)))
; __device__ __forceinline__ float dot4(f32x4 a, f32x4 b) { return (a.x * b.x + a.y * b.y) + (a.z * b.z + a.w * b.w); }
; __device__ __forceinline__ float wave_sum(float v) {
; #pragma unroll
;     for (int o = 1; o < 64; o <<= 1) v += __shfl_xor(v, o);
;     return v;
; }
; __device__ __forceinline__ void phase1(KP kp, LAS unsigned char* lds, int wave, int bid, int G) {
;     ...
;     for (int m = bid * NWAVES + wave; m < T; m += G * NWAVES) {
;         const GAS f32x4* xr = (const GAS f32x4*)(x + (size_t)m * DM) + lane;
;         f32x4 v[8]; float s = 0.f;
; #pragma unroll
;         for (int j = 0; j < 8; ++j) { v[j] = xr[64 * j]; s += dot4(v[j], v[j]); }
;         const float rstd = 1.0f / sqrtf(wave_sum(s) * (1.0f / DM) + EPS);
.LBB0_135:
	global_load_dwordx4 v[64:67], v[82:83], off offset:-3072
	global_load_dwordx4 v[68:71], v[82:83], off offset:-2048
	global_load_dwordx4 v[72:75], v[82:83], off
	global_load_dwordx4 v[76:79], v[82:83], off offset:-1024
	v_add_co_u32_e32 v84, vcc, 0xfffff000, v82
	s_add_i32 s8, s8, s10
	s_nop 0
	v_addc_co_u32_e32 v85, vcc, -1, v83, vcc
	global_load_dwordx4 v[94:97], v[84:85], off offset:-3072
	global_load_dwordx4 v[98:101], v[84:85], off offset:-2048
	global_load_dwordx4 v[102:105], v[84:85], off offset:-1024
	global_load_dwordx4 v[106:109], v[82:83], off offset:-4096
	s_cmpk_lt_i32 s8, 0x2000
	v_lshl_add_u64 v[82:83], v[82:83], 0, s[12:13]
	s_waitcnt vmcnt(7)
	v_mul_f32_e32 v131, v64, v64
	s_waitcnt vmcnt(6)
	v_pk_mul_f32 v[84:85], v[70:71], v[70:71]
	v_pk_mul_f32 v[110:111], v[68:69], v[68:69]
	s_waitcnt vmcnt(4)
	v_mul_f32_e32 v112, v77, v77
	v_mul_f32_e32 v114, v79, v79
	v_mul_f32_e32 v129, v74, v74
	v_mul_f32_e32 v137, v75, v75
	v_pk_mov_b32 v[116:117], v[110:111], v[84:85] op_sel:[1,0]
	v_mov_b32_e32 v111, v85
	v_pk_fma_f32 v[84:85], v[76:77], v[76:77], v[112:113] op_sel_hi:[1,1,0]
	v_pk_fma_f32 v[112:113], v[78:79], v[78:79], v[114:115] op_sel_hi:[1,1,0]
	s_waitcnt vmcnt(3)
	v_mov_b32_e32 v118, v95
	s_waitcnt vmcnt(2)
	v_mov_b32_e32 v119, v99
	v_mov_b32_e32 v122, v97
	v_mov_b32_e32 v123, v101
	v_mov_b32_e32 v114, v94
	v_mov_b32_e32 v115, v98
	v_mov_b32_e32 v120, v96
	v_mov_b32_e32 v121, v100
	s_waitcnt vmcnt(1)
	v_pk_mul_f32 v[124:125], v[104:105], v[104:105]
	v_pk_mul_f32 v[126:127], v[102:103], v[102:103]
	v_pk_add_f32 v[110:111], v[116:117], v[110:111]
	v_mov_b32_e32 v85, v129
	v_mov_b32_e32 v113, v137
	v_pk_mul_f32 v[116:117], v[118:119], v[118:119]
	v_pk_mul_f32 v[118:119], v[122:123], v[122:123]
	v_pk_mov_b32 v[122:123], v[126:127], v[124:125] op_sel:[1,0]
	v_mov_b32_e32 v127, v125
	v_pk_add_f32 v[84:85], v[84:85], v[112:113]
	v_pk_fma_f32 v[112:113], v[114:115], v[114:115], v[116:117]
	v_pk_fma_f32 v[114:115], v[120:121], v[120:121], v[118:119]
	s_waitcnt vmcnt(0)
	v_mul_f32_e32 v128, v107, v107
	v_mul_f32_e32 v130, v109, v109
	v_pk_add_f32 v[116:117], v[122:123], v[126:127]
	v_pk_add_f32 v[112:113], v[112:113], v[114:115]
	v_mul_f32_e32 v132, v65, v65
	v_mul_f32_e32 v133, v66, v66
	v_mul_f32_e32 v134, v67, v67
	v_pk_fma_f32 v[124:125], v[106:107], v[106:107], v[128:129] op_sel_hi:[1,1,0]
	v_pk_fma_f32 v[128:129], v[108:109], v[108:109], v[130:131] op_sel_hi:[1,1,0]
	v_pk_add_f32 v[114:115], v[116:117], v[116:117] op_sel:[0,1] op_sel_hi:[1,0]
	v_pk_add_f32 v[112:113], v[112:113], v[112:113] op_sel:[0,1] op_sel_hi:[1,0]
	v_mov_b32_e32 v125, v133
	v_mov_b32_e32 v129, v134
	v_mov_b32_e32 v115, v132
	v_mov_b32_e32 v113, v131
	v_pk_add_f32 v[116:117], v[124:125], v[128:129]
	v_pk_add_f32 v[112:113], v[112:113], v[114:115]
	v_mul_f32_e32 v135, v72, v72
	v_pk_add_f32 v[112:113], v[112:113], v[116:117]
	v_mul_f32_e32 v136, v73, v73
	v_pk_add_f32 v[110:111], v[110:111], v[110:111] op_sel:[0,1] op_sel_hi:[1,0]
	v_pk_add_f32 v[112:113], v[112:113], v[112:113] op_sel:[0,1] op_sel_hi:[1,0]
	v_mov_b32_e32 v111, v136
	v_mov_b32_e32 v113, v135
	v_pk_add_f32 v[110:111], v[112:113], v[110:111]
	s_nop 0
	v_pk_add_f32 v[84:85], v[110:111], v[84:85]
	s_nop 0
	v_add_f32_e32 v84, v84, v85
	s_nop 1
	v_add_f32_dpp v84, v84, v84 quad_perm:[1,0,3,2] row_mask:0xf bank_mask:0xf
	s_nop 1
	v_add_f32_dpp v84, v84, v84 quad_perm:[2,3,0,1] row_mask:0xf bank_mask:0xf
	s_nop 1
	v_add_f32_dpp v84, v84, v84 row_half_mirror row_mask:0xf bank_mask:0xf
	s_nop 1
	v_add_f32_dpp v84, v84, v84 row_mirror row_mask:0xf bank_mask:0xf
	v_mov_b32_e32 v85, v84
	s_nop 1
	v_permlane16_swap_b32_e32 v84, v85
	v_add_f32_e32 v84, v84, v85
	v_mov_b32_e32 v85, v84
	s_nop 1
	v_permlane32_swap_b32_e32 v84, v85
	v_add_f32_e32 v84, v84, v85
	v_fmamk_f32 v84, v84, 0x3a000000, v92
	v_mul_f32_e32 v85, 0x4f800000, v84
	v_cmp_gt_f32_e32 vcc, s4, v84
	s_nop 1
	v_cndmask_b32_e32 v84, v84, v85, vcc
	v_sqrt_f32_e32 v85, v84
	s_nop 0
	v_add_u32_e32 v110, -1, v85
	v_add_u32_e32 v111, 1, v85
	v_fma_f32 v112, -v110, v85, v84
	v_fma_f32 v113, -v111, v85, v84
	v_cmp_ge_f32_e64 s[2:3], 0, v112
	s_nop 1
	v_cndmask_b32_e64 v85, v85, v110, s[2:3]
	v_cmp_lt_f32_e64 s[2:3], 0, v113
	s_nop 1
	v_cndmask_b32_e64 v85, v85, v111, s[2:3]
	v_mul_f32_e32 v110, 0x37800000, v85
	v_cndmask_b32_e32 v85, v85, v110, vcc
	v_cmp_class_f32_e32 vcc, v84, v93
	s_nop 1
	v_cndmask_b32_e32 v84, v85, v84, vcc
	v_div_scale_f32 v85, s[2:3], v84, v84, 1.0
	v_rcp_f32_e32 v111, v85
	v_div_scale_f32 v110, vcc, 1.0, v84, 1.0
	v_fma_f32 v112, -v85, v111, 1.0
	v_fmac_f32_e32 v111, v112, v111
	v_mul_f32_e32 v112, v110, v111
	v_fma_f32 v113, -v85, v112, v110
	v_fmac_f32_e32 v112, v113, v111
	v_fma_f32 v85, -v85, v112, v110
	v_div_fmas_f32 v85, v85, v111, v112
	v_div_fixup_f32 v84, v85, v84, 1.0
	v_pk_mul_f32 v[94:95], v[94:95], v[84:85] op_sel_hi:[1,0]
	v_pk_mul_f32 v[96:97], v[96:97], v[84:85] op_sel_hi:[1,0]
	v_pk_mul_f32 v[98:99], v[98:99], v[84:85] op_sel_hi:[1,0]
	v_pk_mul_f32 v[100:101], v[100:101], v[84:85] op_sel_hi:[1,0]
; #define GAS __attribute__((address_space(1)))
; #define LAS __attribute__((address_space(3)))
; __device__ __forceinline__ unsigned f2bf(float f) { unsigned u = __builtin_bit_cast(unsigned, f); return (u + 0x7fffu + ((u >> 16) & 1u)) >> 16; }
; __device__ __forceinline__ unsigned pk2(float lo, float hi) { return f2bf(lo) | (f2bf(hi) << 16); }
; __device__ __forceinline__ u32x2 pack4(f32x4 v) { u32x2 w; w.x = pk2(v.x, v.y); w.y = pk2(v.z, v.w); return w; }
; __device__ __forceinline__ void phase1(KP kp, LAS unsigned char* lds, int wave, int bid, int G) {
;     ...
;         GAS u32x2* o8 = (GAS u32x2*)(H + (size_t)m * DM) + lane;
; #pragma unroll
;         for (int j = 0; j < 8; ++j) { const f32x4 av = *(const LAS f32x4*)(A1 + 256 * j + 4 * lane), bv = *(const LAS f32x4*)(B1 + 256 * j + 4 * lane);
;             o8[64 * j] = pack4(v[j] * rstd * av + bv); }
	v_pk_mul_f32 v[102:103], v[102:103], v[84:85] op_sel_hi:[1,0]
	v_pk_mul_f32 v[104:105], v[104:105], v[84:85] op_sel_hi:[1,0]
	v_pk_mul_f32 v[106:107], v[106:107], v[84:85] op_sel_hi:[1,0]
	v_pk_mul_f32 v[108:109], v[108:109], v[84:85] op_sel_hi:[1,0]
	v_pk_mul_f32 v[64:65], v[64:65], v[84:85] op_sel_hi:[1,0]
	v_pk_mul_f32 v[66:67], v[66:67], v[84:85] op_sel_hi:[1,0]
	v_pk_mul_f32 v[68:69], v[68:69], v[84:85] op_sel_hi:[1,0]
	v_pk_mul_f32 v[70:71], v[70:71], v[84:85] op_sel_hi:[1,0]
	v_pk_mul_f32 v[76:77], v[76:77], v[84:85] op_sel_hi:[1,0]
	v_pk_mul_f32 v[78:79], v[78:79], v[84:85] op_sel_hi:[1,0]
	v_pk_mul_f32 v[72:73], v[72:73], v[84:85] op_sel_hi:[1,0]
	v_pk_mul_f32 v[74:75], v[74:75], v[84:85] op_sel_hi:[1,0]
	v_pk_fma_f32 v[84:85], v[2:3], v[96:97], v[10:11]
	v_pk_fma_f32 v[94:95], v[0:1], v[94:95], v[8:9]
	v_pk_fma_f32 v[96:97], v[6:7], v[100:101], v[14:15]
	v_pk_fma_f32 v[98:99], v[4:5], v[98:99], v[12:13]
	v_pk_fma_f32 v[100:101], v[18:19], v[104:105], v[26:27]
	v_pk_fma_f32 v[102:103], v[16:17], v[102:103], v[24:25]
	v_pk_fma_f32 v[104:105], v[22:23], v[108:109], v[30:31]
	v_pk_fma_f32 v[106:107], v[20:21], v[106:107], v[28:29]
	v_pk_fma_f32 v[66:67], v[34:35], v[66:67], v[42:43]
	v_pk_fma_f32 v[64:65], v[32:33], v[64:65], v[40:41]
	v_pk_fma_f32 v[70:71], v[38:39], v[70:71], v[46:47]
	v_pk_fma_f32 v[68:69], v[36:37], v[68:69], v[44:45]
	v_pk_fma_f32 v[78:79], v[50:51], v[78:79], v[58:59]
	v_pk_fma_f32 v[76:77], v[48:49], v[76:77], v[56:57]
	v_pk_fma_f32 v[74:75], v[54:55], v[74:75], v[62:63]
	v_pk_fma_f32 v[72:73], v[52:53], v[72:73], v[60:61]
	v_bfe_u32 v108, v94, 16, 1
	v_bfe_u32 v110, v84, 16, 1
	v_bfe_u32 v109, v95, 16, 1
	v_bfe_u32 v111, v85, 16, 1
	v_bfe_u32 v112, v98, 16, 1
	v_bfe_u32 v114, v96, 16, 1
	v_bfe_u32 v116, v102, 16, 1
	v_bfe_u32 v118, v100, 16, 1
	v_bfe_u32 v120, v106, 16, 1
	v_bfe_u32 v122, v104, 16, 1
	v_bfe_u32 v124, v64, 16, 1
	v_bfe_u32 v125, v65, 16, 1
	v_bfe_u32 v126, v66, 16, 1
	v_bfe_u32 v127, v67, 16, 1
	v_bfe_u32 v128, v68, 16, 1
	v_bfe_u32 v129, v69, 16, 1
	v_bfe_u32 v130, v70, 16, 1
	v_bfe_u32 v131, v71, 16, 1
	v_bfe_u32 v132, v76, 16, 1
	v_bfe_u32 v134, v78, 16, 1
	v_bfe_u32 v136, v72, 16, 1
	v_bfe_u32 v137, v73, 16, 1
	v_bfe_u32 v138, v74, 16, 1
	v_add3_u32 v94, v94, v108, s5
	v_add3_u32 v84, v84, v110, s5
	v_bfe_u32 v113, v99, 16, 1
	v_bfe_u32 v115, v97, 16, 1
	v_bfe_u32 v117, v103, 16, 1
	v_bfe_u32 v119, v101, 16, 1
	v_bfe_u32 v121, v107, 16, 1
	v_bfe_u32 v123, v105, 16, 1
	v_bfe_u32 v133, v77, 16, 1
	v_bfe_u32 v135, v79, 16, 1
	v_bfe_u32 v139, v75, 16, 1
	v_add3_u32 v95, v95, v109, s5
	v_add3_u32 v85, v85, v111, s5
	v_add3_u32 v98, v98, v112, s5
	v_add3_u32 v96, v96, v114, s5
	v_add3_u32 v102, v102, v116, s5
	v_add3_u32 v100, v100, v118, s5
	v_add3_u32 v106, v106, v120, s5
	v_add3_u32 v104, v104, v122, s5
	v_add3_u32 v64, v64, v124, s5
	v_add3_u32 v108, v65, v125, s5
	v_add3_u32 v65, v66, v126, s5
	v_add3_u32 v109, v67, v127, s5
	v_add3_u32 v66, v68, v128, s5
	v_add3_u32 v110, v69, v129, s5
	v_add3_u32 v67, v70, v130, s5
	v_add3_u32 v111, v71, v131, s5
	v_add3_u32 v68, v76, v132, s5
	v_add3_u32 v69, v78, v134, s5
	v_add3_u32 v70, v72, v136, s5
	v_add3_u32 v78, v73, v137, s5
	v_add3_u32 v71, v74, v138, s5
	v_lshrrev_b32_e32 v72, 16, v94
	v_lshrrev_b32_e32 v73, 16, v84
	v_add3_u32 v99, v99, v113, s5
	v_add3_u32 v97, v97, v115, s5
	v_add3_u32 v103, v103, v117, s5
	v_add3_u32 v101, v101, v119, s5
	v_add3_u32 v107, v107, v121, s5
	v_add3_u32 v105, v105, v123, s5
	v_add3_u32 v76, v77, v133, s5
	v_add3_u32 v77, v79, v135, s5
	v_add3_u32 v79, v75, v139, s5
	v_lshrrev_b32_e32 v74, 16, v98
	v_lshrrev_b32_e32 v75, 16, v96
	v_lshrrev_b32_e32 v84, 16, v102
	v_lshrrev_b32_e32 v94, 16, v100
	v_lshrrev_b32_e32 v96, 16, v106
	v_lshrrev_b32_e32 v98, 16, v104
	v_lshrrev_b32_e32 v100, 16, v64
	v_lshrrev_b32_e32 v102, 16, v65
	v_lshrrev_b32_e32 v104, 16, v66
	v_lshrrev_b32_e32 v106, 16, v67
	v_lshrrev_b32_e32 v112, 16, v68
	v_lshrrev_b32_e32 v113, 16, v69
	v_lshrrev_b32_e32 v114, 16, v70
	v_lshrrev_b32_e32 v115, 16, v71
	v_and_or_b32 v64, v95, s9, v72
	v_and_or_b32 v65, v85, s9, v73
	v_and_or_b32 v66, v99, s9, v74
	v_and_or_b32 v67, v97, s9, v75
	v_and_or_b32 v68, v103, s9, v84
	v_and_or_b32 v69, v101, s9, v94
	v_and_or_b32 v70, v107, s9, v96
	v_and_or_b32 v71, v105, s9, v98
	v_and_or_b32 v72, v108, s9, v100
	v_and_or_b32 v73, v109, s9, v102
	v_and_or_b32 v74, v110, s9, v104
	v_and_or_b32 v75, v111, s9, v106
	v_and_or_b32 v76, v76, s9, v112
	v_and_or_b32 v77, v77, s9, v113
	v_and_or_b32 v78, v78, s9, v114
	v_and_or_b32 v79, v79, s9, v115
	global_store_dwordx2 v[80:81], v[64:65], off offset:-3584
	global_store_dwordx2 v[80:81], v[66:67], off offset:-3072
	global_store_dwordx2 v[80:81], v[68:69], off offset:-2560
	global_store_dwordx2 v[80:81], v[70:71], off offset:-2048
	global_store_dwordx2 v[80:81], v[72:73], off offset:-1536
	global_store_dwordx2 v[80:81], v[74:75], off offset:-1024
	global_store_dwordx2 v[80:81], v[76:77], off offset:-512
	global_store_dwordx2 v[80:81], v[78:79], off
	v_lshl_add_u64 v[80:81], v[80:81], 0, s[6:7]
	s_cbranch_scc1 .LBB0_135

; #define GAS __attribute__((address_space(1)))
; __device__ __forceinline__ float dot4(f32x4 a, f32x4 b) { return (a.x * b.x + a.y * b.y) + (a.z * b.z + a.w * b.w); }
; __device__ __forceinline__ u32x2 pack4(f32x4 v) { u32x2 w; w.x = pk2(v.x, v.y); w.y = pk2(v.z, v.w); return w; }
; __device__ __forceinline__ f32x4 unpack4(u32x2 w) { return (f32x4){bflo(w.x), bfhi(w.x), bflo(w.y), bfhi(w.y)}; }
; __device__ __forceinline__ float wave_sum(float v) {
; #pragma unroll
;     for (int o = 1; o < 64; o <<= 1) v += __shfl_xor(v, o);
;     return v;
; }
; __device__ __forceinline__ void phase4(KP kp, int wave, int bid, int G) {
;     ...
;     for (int it = gw; it < T * 8; it += NGW) { const int t = it >> 3, hd = it & 7;
;         const bf16* o0 = OA + (size_t)t * 4096 + hd * 512 + 4 * lane;
;         const f32x4 d = unpack4(*(const GAS u32x2*)o0) - lam * unpack4(*(const GAS u32x2*)(o0 + 256));
;         const float rstd = 1.0f / sqrtf(wave_sum(dot4(d, d)) * (1.0f / 256.0f) + EPS);
;         *(GAS u32x2*)(ON + (size_t)t * 4096 + hd * 256 + 4 * lane) = pack4(d * rstd * sg); }
.LBB0_709:
	s_ashr_i32 s2, s9, 3
	s_ashr_i32 s3, s2, 31
	s_lshl_b64 s[2:3], s[2:3], 13
	v_xor_b32_e32 v11, 0x80000000, v3
	v_lshl_add_u64 v[22:23], v[6:7], 0, s[2:3]
	s_lshl_b32 s24, s18, 1
	s_add_i32 s24, s24, s9
	s_min_i32 s24, s24, 0xffff
	s_ashr_i32 s22, s24, 3
	s_ashr_i32 s23, s22, 31
	s_lshl_b64 s[22:23], s[22:23], 13
	v_lshl_add_u64 v[60:61], v[4:5], 0, s[22:23]
	s_add_i32 s9, s9, s18
	s_waitcnt vmcnt(4)
	v_lshlrev_b32_e32 v28, 16, v56
	v_and_b32_e32 v29, 0xffff0000, v56
	v_lshlrev_b32_e32 v24, 16, v57
	v_and_b32_e32 v25, 0xffff0000, v57
	v_lshlrev_b32_e32 v30, 16, v58
	v_and_b32_e32 v31, 0xffff0000, v58
	v_lshlrev_b32_e32 v26, 16, v59
	v_and_b32_e32 v27, 0xffff0000, v59
	global_load_dwordx2 v[56:57], v[60:61], off
	global_load_dwordx2 v[58:59], v[60:61], off offset:512
	v_pk_fma_f32 v[28:29], v[8:9], v[30:31], v[28:29] neg_lo:[1,0,0] neg_hi:[1,0,0]
	v_pk_fma_f32 v[24:25], v[10:11], v[26:27], v[24:25]
	v_pk_mul_f32 v[30:31], v[28:29], v[28:29]
	v_pk_mul_f32 v[26:27], v[24:25], v[24:25]
	s_nop 0
	v_pk_mov_b32 v[32:33], v[30:31], v[26:27] op_sel:[1,0]
	v_mov_b32_e32 v31, v27
	v_pk_add_f32 v[26:27], v[32:33], v[30:31]
	s_nop 0
	v_add_f32_e32 v11, v26, v27
	s_nop 1
	v_add_f32_dpp v11, v11, v11 quad_perm:[1,0,3,2] row_mask:0xf bank_mask:0xf
	s_nop 1
	v_add_f32_dpp v11, v11, v11 quad_perm:[2,3,0,1] row_mask:0xf bank_mask:0xf
	s_nop 1
	v_add_f32_dpp v11, v11, v11 row_half_mirror row_mask:0xf bank_mask:0xf
	s_nop 1
	v_add_f32_dpp v11, v11, v11 row_mirror row_mask:0xf bank_mask:0xf
	v_mov_b32_e32 v26, v11
	s_nop 1
	v_permlane16_swap_b32_e32 v11, v26
	v_add_f32_e32 v11, v11, v26
	v_mov_b32_e32 v26, v11
	s_nop 1
	v_permlane32_swap_b32_e32 v11, v26
	v_add_f32_e32 v11, v11, v26
	v_fmamk_f32 v11, v11, 0x3b800000, v20
	v_mul_f32_e32 v26, 0x4f800000, v11
	v_cmp_gt_f32_e32 vcc, s5, v11
	s_nop 1
	v_cndmask_b32_e32 v11, v11, v26, vcc
	v_sqrt_f32_e32 v26, v11
	s_nop 0
	v_add_u32_e32 v27, -1, v26
	v_add_u32_e32 v30, 1, v26
	v_fma_f32 v31, -v27, v26, v11
	v_fma_f32 v32, -v30, v26, v11
	v_cmp_ge_f32_e64 s[2:3], 0, v31
	s_nop 1
	v_cndmask_b32_e64 v26, v26, v27, s[2:3]
	v_cmp_lt_f32_e64 s[2:3], 0, v32
	s_nop 1
	v_cndmask_b32_e64 v26, v26, v30, s[2:3]
	v_mul_f32_e32 v27, 0x37800000, v26
	v_cndmask_b32_e32 v26, v26, v27, vcc
	v_cmp_class_f32_e32 vcc, v11, v21
	s_nop 1
	v_cndmask_b32_e32 v11, v26, v11, vcc
	v_div_scale_f32 v26, s[2:3], v11, v11, 1.0
	v_rcp_f32_e32 v30, v26
	v_div_scale_f32 v27, vcc, 1.0, v11, 1.0
	v_fma_f32 v31, -v26, v30, 1.0
	v_fmac_f32_e32 v30, v31, v30
	v_mul_f32_e32 v31, v27, v30
	v_fma_f32 v32, -v26, v31, v27
	v_fmac_f32_e32 v31, v32, v30
	v_fma_f32 v26, -v26, v31, v27
	v_div_fmas_f32 v26, v26, v30, v31
	v_div_fixup_f32 v26, v26, v11, 1.0
	v_pk_mul_f32 v[28:29], v[28:29], v[26:27] op_sel_hi:[1,0]
	v_pk_mul_f32 v[24:25], v[24:25], v[26:27] op_sel_hi:[1,0]
	v_pk_mul_f32 v[26:27], v[14:15], v[28:29]
	v_pk_mul_f32 v[24:25], v[12:13], v[24:25]
	v_bfe_u32 v11, v26, 16, 1
	v_bfe_u32 v29, v24, 16, 1
	v_bfe_u32 v28, v27, 16, 1
	v_bfe_u32 v30, v25, 16, 1
	v_add3_u32 v11, v26, v11, s8
	v_add3_u32 v24, v24, v29, s8
	v_add3_u32 v26, v27, v28, s8
	v_add3_u32 v25, v25, v30, s8
	v_lshrrev_b32_e32 v11, 16, v11
	v_lshrrev_b32_e32 v27, 16, v24
	v_and_or_b32 v24, v26, s4, v11
	v_and_or_b32 v25, v25, s4, v27
	global_store_dwordx2 v[22:23], v[24:25], off
	s_cmp_gt_i32 s9, 0xffff
	s_cbranch_scc1 .Lp4_exit
	s_ashr_i32 s2, s9, 3
	s_ashr_i32 s3, s2, 31
	s_lshl_b64 s[2:3], s[2:3], 13
	v_xor_b32_e32 v11, 0x80000000, v3
	v_lshl_add_u64 v[22:23], v[6:7], 0, s[2:3]
	s_lshl_b32 s24, s18, 1
	s_add_i32 s24, s24, s9
	s_min_i32 s24, s24, 0xffff
	s_ashr_i32 s22, s24, 3
	s_ashr_i32 s23, s22, 31
	s_lshl_b64 s[22:23], s[22:23], 13
	v_lshl_add_u64 v[60:61], v[4:5], 0, s[22:23]
	s_add_i32 s9, s9, s18
	s_waitcnt vmcnt(4)
	v_lshlrev_b32_e32 v28, 16, v62
	v_and_b32_e32 v29, 0xffff0000, v62
	v_lshlrev_b32_e32 v24, 16, v63
	v_and_b32_e32 v25, 0xffff0000, v63
	v_lshlrev_b32_e32 v30, 16, v64
	v_and_b32_e32 v31, 0xffff0000, v64
	v_lshlrev_b32_e32 v26, 16, v65
	v_and_b32_e32 v27, 0xffff0000, v65
	global_load_dwordx2 v[62:63], v[60:61], off
	global_load_dwordx2 v[64:65], v[60:61], off offset:512
	v_pk_fma_f32 v[28:29], v[8:9], v[30:31], v[28:29] neg_lo:[1,0,0] neg_hi:[1,0,0]
	v_pk_fma_f32 v[24:25], v[10:11], v[26:27], v[24:25]
	v_pk_mul_f32 v[30:31], v[28:29], v[28:29]
	v_pk_mul_f32 v[26:27], v[24:25], v[24:25]
	s_nop 0
	v_pk_mov_b32 v[32:33], v[30:31], v[26:27] op_sel:[1,0]
	v_mov_b32_e32 v31, v27
	v_pk_add_f32 v[26:27], v[32:33], v[30:31]
	s_nop 0
	v_add_f32_e32 v11, v26, v27
	s_nop 1
	v_add_f32_dpp v11, v11, v11 quad_perm:[1,0,3,2] row_mask:0xf bank_mask:0xf
	s_nop 1
	v_add_f32_dpp v11, v11, v11 quad_perm:[2,3,0,1] row_mask:0xf bank_mask:0xf
	s_nop 1
	v_add_f32_dpp v11, v11, v11 row_half_mirror row_mask:0xf bank_mask:0xf
	s_nop 1
	v_add_f32_dpp v11, v11, v11 row_mirror row_mask:0xf bank_mask:0xf
	v_mov_b32_e32 v26, v11
	s_nop 1
	v_permlane16_swap_b32_e32 v11, v26
	v_add_f32_e32 v11, v11, v26
	v_mov_b32_e32 v26, v11
	s_nop 1
	v_permlane32_swap_b32_e32 v11, v26
	v_add_f32_e32 v11, v11, v26
	v_fmamk_f32 v11, v11, 0x3b800000, v20
	v_mul_f32_e32 v26, 0x4f800000, v11
	v_cmp_gt_f32_e32 vcc, s5, v11
	s_nop 1
	v_cndmask_b32_e32 v11, v11, v26, vcc
	v_sqrt_f32_e32 v26, v11
	s_nop 0
	v_add_u32_e32 v27, -1, v26
	v_add_u32_e32 v30, 1, v26
	v_fma_f32 v31, -v27, v26, v11
	v_fma_f32 v32, -v30, v26, v11
	v_cmp_ge_f32_e64 s[2:3], 0, v31
	s_nop 1
	v_cndmask_b32_e64 v26, v26, v27, s[2:3]
	v_cmp_lt_f32_e64 s[2:3], 0, v32
	s_nop 1
	v_cndmask_b32_e64 v26, v26, v30, s[2:3]
	v_mul_f32_e32 v27, 0x37800000, v26
	v_cndmask_b32_e32 v26, v26, v27, vcc
	v_cmp_class_f32_e32 vcc, v11, v21
	s_nop 1
	v_cndmask_b32_e32 v11, v26, v11, vcc
	v_div_scale_f32 v26, s[2:3], v11, v11, 1.0
	v_rcp_f32_e32 v30, v26
	v_div_scale_f32 v27, vcc, 1.0, v11, 1.0
	v_fma_f32 v31, -v26, v30, 1.0
	v_fmac_f32_e32 v30, v31, v30
	v_mul_f32_e32 v31, v27, v30
	v_fma_f32 v32, -v26, v31, v27
	v_fmac_f32_e32 v31, v32, v30
	v_fma_f32 v26, -v26, v31, v27
	v_div_fmas_f32 v26, v26, v30, v31
	v_div_fixup_f32 v26, v26, v11, 1.0
	v_pk_mul_f32 v[28:29], v[28:29], v[26:27] op_sel_hi:[1,0]
	v_pk_mul_f32 v[24:25], v[24:25], v[26:27] op_sel_hi:[1,0]
	v_pk_mul_f32 v[26:27], v[14:15], v[28:29]
	v_pk_mul_f32 v[24:25], v[12:13], v[24:25]
	v_bfe_u32 v11, v26, 16, 1
	v_bfe_u32 v29, v24, 16, 1
	v_bfe_u32 v28, v27, 16, 1
	v_bfe_u32 v30, v25, 16, 1
	v_add3_u32 v11, v26, v11, s8
	v_add3_u32 v24, v24, v29, s8
	v_add3_u32 v26, v27, v28, s8
	v_add3_u32 v25, v25, v30, s8
	v_lshrrev_b32_e32 v11, 16, v11
	v_lshrrev_b32_e32 v27, 16, v24
	v_and_or_b32 v24, v26, s4, v11
	v_and_or_b32 v25, v25, s4, v27
	global_store_dwordx2 v[22:23], v[24:25], off
	s_cmp_gt_i32 s9, 0xffff
	s_cbranch_scc0 .LBB0_709

; #define GAS __attribute__((address_space(1)))
; #define LAS __attribute__((address_space(3)))
; __device__ __forceinline__ float dot4(f32x4 a, f32x4 b) { return (a.x * b.x + a.y * b.y) + (a.z * b.z + a.w * b.w); }
; __device__ __forceinline__ u32x2 pack4(f32x4 v) { u32x2 w; w.x = pk2(v.x, v.y); w.y = pk2(v.z, v.w); return w; }
; __device__ __forceinline__ float wave_sum(float v) {
; #pragma unroll
;     for (int o = 1; o < 64; o <<= 1) v += __shfl_xor(v, o);
;     return v;
; }
; __device__ __forceinline__ void phase8(KP kp, LAS unsigned char* lds, int wave, int bid) {
;     ...
;     for (int q = 0; q < 4; ++q) {
;         const int lt = 4 * wave + q, t = 32 * bid + lt;
;         const GAS f32x4* xr = (const GAS f32x4*)(X1 + (size_t)t * DM) + lane;
;         f32x4 v[8]; float s = 0.f;
; #pragma unroll
;         for (int j = 0; j < 8; ++j) { v[j] = xr[64 * j]; s += dot4(v[j], v[j]); }
;         const float rstd = 1.0f / sqrtf(wave_sum(s) * (1.0f / DM) + EPS);
;         if (lane == 0) rs[lt] = rstd;
;         GAS u32x2* o8 = (GAS u32x2*)(H + (size_t)t * DM) + lane;
; #pragma unroll
;         for (int j = 0; j < 8; ++j) { const f32x4 av = *(const LAS f32x4*)(A2 + 256 * j + 4 * lane), bv = *(const LAS f32x4*)(B2 + 256 * j + 4 * lane);
;             o8[64 * j] = pack4(v[j] * rstd * av + bv); }
.LBB0_933:
	v_lshl_add_u64 v[42:43], s[8:9], 0, v[38:39]
	v_add_co_u32_e32 v16, vcc, s20, v42
	s_nop 1
	v_addc_co_u32_e32 v17, vcc, 0, v43, vcc
	global_load_dwordx4 v[12:15], v[16:17], off
	v_add_co_u32_e32 v40, vcc, 0x56000000, v42
	global_load_dwordx4 v[8:11], v[16:17], off offset:1024
	global_load_dwordx4 v[4:7], v[16:17], off offset:2048
	global_load_dwordx4 v[0:3], v[16:17], off offset:3072
	v_addc_co_u32_e32 v41, vcc, 0, v43, vcc
	global_load_dwordx4 v[28:31], v[40:41], off
	global_load_dwordx4 v[24:27], v[40:41], off offset:1024
	global_load_dwordx4 v[20:23], v[40:41], off offset:2048
	global_load_dwordx4 v[16:19], v[40:41], off offset:3072
	s_waitcnt vmcnt(7)
	v_mul_f32_e32 v40, v13, v13
	v_mul_f32_e32 v41, v15, v15
	s_waitcnt vmcnt(6)
	v_mul_f32_e32 v44, v9, v9
	v_mul_f32_e32 v52, v11, v11
	s_waitcnt vmcnt(5)
	v_mul_f32_e32 v53, v5, v5
	v_mul_f32_e32 v54, v7, v7
	s_waitcnt vmcnt(3)
	v_mul_f32_e32 v57, v29, v29
	v_mul_f32_e32 v58, v31, v31
	s_waitcnt vmcnt(2)
	v_mul_f32_e32 v59, v25, v25
	v_mul_f32_e32 v60, v27, v27
	v_mul_f32_e32 v55, v1, v1
	v_mul_f32_e32 v56, v3, v3
	s_waitcnt vmcnt(1)
	v_mul_f32_e32 v61, v21, v21
	v_mul_f32_e32 v62, v23, v23
	v_fmac_f32_e32 v40, v12, v12
	v_fmac_f32_e32 v41, v14, v14
	v_fmac_f32_e32 v44, v8, v8
	v_fmac_f32_e32 v52, v10, v10
	v_fmac_f32_e32 v53, v4, v4
	v_fmac_f32_e32 v54, v6, v6
	v_fmac_f32_e32 v57, v28, v28
	v_fmac_f32_e32 v58, v30, v30
	v_fmac_f32_e32 v59, v24, v24
	v_fmac_f32_e32 v60, v26, v26
	s_waitcnt vmcnt(0)
	v_mul_f32_e32 v63, v17, v17
	v_mul_f32_e32 v64, v19, v19
	v_fmac_f32_e32 v55, v0, v0
	v_fmac_f32_e32 v56, v2, v2
	v_fmac_f32_e32 v61, v20, v20
	v_fmac_f32_e32 v62, v22, v22
	v_add_f32_e32 v40, v40, v41
	v_add_f32_e32 v41, v44, v52
	v_add_f32_e32 v44, v53, v54
	v_add_f32_e32 v53, v57, v58
	v_add_f32_e32 v54, v59, v60
	v_fmac_f32_e32 v63, v16, v16
	v_fmac_f32_e32 v64, v18, v18
	v_add_f32_e32 v52, v55, v56
	v_add_f32_e32 v55, v61, v62
	v_add_f32_e32 v53, v53, v54
	v_add_f32_e32 v56, v63, v64
	v_add_f32_e32 v53, v53, v55
	v_add_f32_e32 v53, v53, v56
	v_add_f32_e32 v40, v53, v40
	v_add_f32_e32 v40, v40, v41
	v_add_f32_e32 v40, v40, v44
	v_add_f32_e32 v40, v40, v52
	s_nop 1
	v_add_f32_dpp v40, v40, v40 quad_perm:[1,0,3,2] row_mask:0xf bank_mask:0xf
	s_nop 1
	v_add_f32_dpp v40, v40, v40 quad_perm:[2,3,0,1] row_mask:0xf bank_mask:0xf
	s_nop 1
	v_add_f32_dpp v40, v40, v40 row_half_mirror row_mask:0xf bank_mask:0xf
	s_nop 1
	v_add_f32_dpp v40, v40, v40 row_mirror row_mask:0xf bank_mask:0xf
	v_mov_b32_e32 v41, v40
	s_nop 1
	v_permlane16_swap_b32_e32 v40, v41
	v_add_f32_e32 v40, v40, v41
	v_mov_b32_e32 v41, v40
	s_nop 1
	v_permlane32_swap_b32_e32 v40, v41
	v_add_f32_e32 v40, v40, v41
	v_fmamk_f32 v40, v40, 0x3a000000, v35
	v_mul_f32_e32 v41, 0x4f800000, v40
	v_cmp_gt_f32_e32 vcc, s21, v40
	s_nop 1
	v_cndmask_b32_e32 v40, v40, v41, vcc
	v_sqrt_f32_e32 v41, v40
	s_nop 0
	v_add_u32_e32 v44, -1, v41
	v_add_u32_e32 v52, 1, v41
	v_fma_f32 v53, -v44, v41, v40
	v_fma_f32 v54, -v52, v41, v40
	v_cmp_ge_f32_e64 s[6:7], 0, v53
	s_nop 1
	v_cndmask_b32_e64 v41, v41, v44, s[6:7]
	v_cmp_lt_f32_e64 s[6:7], 0, v54
	s_nop 1
	v_cndmask_b32_e64 v41, v41, v52, s[6:7]
	v_mul_f32_e32 v44, 0x37800000, v41
	v_cndmask_b32_e32 v41, v41, v44, vcc
	v_cmp_class_f32_e32 vcc, v40, v51
	s_nop 1
	v_cndmask_b32_e32 v40, v41, v40, vcc
	v_div_scale_f32 v41, s[6:7], v40, v40, 1.0
	v_rcp_f32_e32 v44, v41
	v_div_scale_f32 v52, vcc, 1.0, v40, 1.0
	v_fma_f32 v53, -v41, v44, 1.0
	v_fmac_f32_e32 v44, v53, v44
	v_mul_f32_e32 v53, v52, v44
	v_fma_f32 v54, -v41, v53, v52
	v_fmac_f32_e32 v53, v54, v44
	v_fma_f32 v41, -v41, v53, v52
	v_div_fmas_f32 v41, v41, v44, v53
	v_div_fixup_f32 v44, v41, v40, 1.0
	s_and_saveexec_b64 s[6:7], s[2:3]
	s_add_i32 s4, s5, s18
	v_mov_b32_e32 v40, s4
	ds_write_b32 v40, v44
	s_or_b64 exec, exec, s[6:7]
	ds_read_b128 v[52:55], v50
	ds_read_b128 v[56:59], v50 offset:8192
	v_pk_mul_f32 v[64:65], v[30:31], v[44:45] op_sel_hi:[1,0]
	v_pk_mul_f32 v[66:67], v[28:29], v[44:45] op_sel_hi:[1,0]
	ds_read_b128 v[28:31], v50 offset:1024
	ds_read_b128 v[60:63], v50 offset:9216
	v_pk_mul_f32 v[24:25], v[24:25], v[44:45] op_sel_hi:[1,0]
	s_waitcnt lgkmcnt(2)
	v_pk_fma_f32 v[52:53], v[66:67], v[52:53], v[56:57]
	v_pk_mul_f32 v[26:27], v[26:27], v[44:45] op_sel_hi:[1,0]
	v_bfe_u32 v56, v52, 16, 1
	s_waitcnt lgkmcnt(0)
	v_pk_fma_f32 v[24:25], v[24:25], v[28:29], v[60:61]
	v_add3_u32 v52, v52, v56, s22
	v_bfe_u32 v28, v24, 16, 1
	v_bfe_u32 v56, v53, 16, 1
	v_add3_u32 v24, v24, v28, s22
	v_bfe_u32 v28, v25, 16, 1
	v_pk_fma_f32 v[54:55], v[64:65], v[54:55], v[58:59]
	v_lshrrev_b32_e32 v52, 16, v52
	v_add3_u32 v53, v53, v56, s22
	v_pk_fma_f32 v[26:27], v[26:27], v[30:31], v[62:63]
	v_lshrrev_b32_e32 v24, 16, v24
	v_add3_u32 v25, v25, v28, s22
	v_and_or_b32 v52, v53, s23, v52
	v_bfe_u32 v53, v54, 16, 1
	v_and_or_b32 v24, v25, s23, v24
	v_bfe_u32 v25, v26, 16, 1
	v_lshl_add_u64 v[40:41], s[8:9], 0, v[36:37]
	v_add3_u32 v53, v54, v53, s22
	v_bfe_u32 v54, v55, 16, 1
	v_add3_u32 v25, v26, v25, s22
	v_bfe_u32 v26, v27, 16, 1
	v_lshrrev_b32_e32 v53, 16, v53
	v_add3_u32 v54, v55, v54, s22
	v_add_co_u32_e32 v56, vcc, s24, v40
	v_lshrrev_b32_e32 v25, 16, v25
	v_add3_u32 v26, v27, v26, s22
	v_and_or_b32 v53, v54, s23, v53
	v_addc_co_u32_e32 v57, vcc, 0, v41, vcc
	v_and_or_b32 v25, v26, s23, v25
	global_store_dwordx2 v[56:57], v[52:53], off
	global_store_dwordx2 v[56:57], v[24:25], off offset:512
	ds_read_b128 v[24:27], v50 offset:2048
	ds_read_b128 v[28:31], v50 offset:10240
	v_pk_mul_f32 v[58:59], v[22:23], v[44:45] op_sel_hi:[1,0]
	v_pk_mul_f32 v[60:61], v[20:21], v[44:45] op_sel_hi:[1,0]
	ds_read_b128 v[20:23], v50 offset:3072
	ds_read_b128 v[52:55], v50 offset:11264
	v_pk_mul_f32 v[16:17], v[16:17], v[44:45] op_sel_hi:[1,0]
	s_waitcnt lgkmcnt(2)
; #define GAS __attribute__((address_space(1)))
; #define LAS __attribute__((address_space(3)))
; __device__ __forceinline__ float dot4(f32x4 a, f32x4 b) { return (a.x * b.x + a.y * b.y) + (a.z * b.z + a.w * b.w); }
; __device__ __forceinline__ u32x2 pack4(f32x4 v) { u32x2 w; w.x = pk2(v.x, v.y); w.y = pk2(v.z, v.w); return w; }
; __device__ __forceinline__ void phase8(KP kp, LAS unsigned char* lds, int wave, int bid) {
;     ...
;         const GAS f32x4* xr = (const GAS f32x4*)(X1 + (size_t)t * DM) + lane;
;         f32x4 v[8]; float s = 0.f;
; #pragma unroll
;         for (int j = 0; j < 8; ++j) { v[j] = xr[64 * j]; s += dot4(v[j], v[j]); }
;     ...
;         GAS u32x2* o8 = (GAS u32x2*)(H + (size_t)t * DM) + lane;
; #pragma unroll
;         for (int j = 0; j < 8; ++j) { const f32x4 av = *(const LAS f32x4*)(A2 + 256 * j + 4 * lane), bv = *(const LAS f32x4*)(B2 + 256 * j + 4 * lane);
;             o8[64 * j] = pack4(v[j] * rstd * av + bv); }
	v_pk_fma_f32 v[24:25], v[60:61], v[24:25], v[28:29]
	v_pk_mul_f32 v[18:19], v[18:19], v[44:45] op_sel_hi:[1,0]
	v_bfe_u32 v28, v24, 16, 1
	s_waitcnt lgkmcnt(0)
	v_pk_fma_f32 v[16:17], v[16:17], v[20:21], v[52:53]
	v_add3_u32 v24, v24, v28, s22
	v_bfe_u32 v20, v16, 16, 1
	v_bfe_u32 v28, v25, 16, 1
	v_add3_u32 v16, v16, v20, s22
	v_bfe_u32 v20, v17, 16, 1
	v_pk_fma_f32 v[26:27], v[58:59], v[26:27], v[30:31]
	v_lshrrev_b32_e32 v24, 16, v24
	v_add3_u32 v25, v25, v28, s22
	v_pk_fma_f32 v[18:19], v[18:19], v[22:23], v[54:55]
	v_lshrrev_b32_e32 v16, 16, v16
	v_add3_u32 v17, v17, v20, s22
	v_and_or_b32 v24, v25, s23, v24
	v_bfe_u32 v25, v26, 16, 1
	v_and_or_b32 v16, v17, s23, v16
	v_bfe_u32 v17, v18, 16, 1
	v_add3_u32 v25, v26, v25, s22
	v_bfe_u32 v26, v27, 16, 1
	v_add3_u32 v17, v18, v17, s22
	v_bfe_u32 v18, v19, 16, 1
	v_lshrrev_b32_e32 v25, 16, v25
	v_add3_u32 v26, v27, v26, s22
	v_lshrrev_b32_e32 v17, 16, v17
	v_add3_u32 v18, v19, v18, s22
	v_and_or_b32 v25, v26, s23, v25
	v_and_or_b32 v17, v18, s23, v17
	global_store_dwordx2 v[56:57], v[24:25], off offset:1024
	global_store_dwordx2 v[56:57], v[16:17], off offset:1536
	ds_read_b128 v[16:19], v50 offset:4096
	ds_read_b128 v[20:23], v50 offset:12288
	v_pk_mul_f32 v[28:29], v[14:15], v[44:45] op_sel_hi:[1,0]
	v_pk_mul_f32 v[30:31], v[12:13], v[44:45] op_sel_hi:[1,0]
	ds_read_b128 v[12:15], v50 offset:5120
	ds_read_b128 v[24:27], v50 offset:13312
	v_pk_mul_f32 v[8:9], v[8:9], v[44:45] op_sel_hi:[1,0]
	s_waitcnt lgkmcnt(2)
	v_pk_fma_f32 v[16:17], v[30:31], v[16:17], v[20:21]
	v_pk_mul_f32 v[10:11], v[10:11], v[44:45] op_sel_hi:[1,0]
	v_bfe_u32 v20, v16, 16, 1
	s_waitcnt lgkmcnt(0)
	v_pk_fma_f32 v[8:9], v[8:9], v[12:13], v[24:25]
	v_add3_u32 v16, v16, v20, s22
	v_bfe_u32 v12, v8, 16, 1
	v_bfe_u32 v20, v17, 16, 1
	v_add3_u32 v8, v8, v12, s22
	v_bfe_u32 v12, v9, 16, 1
	v_pk_fma_f32 v[18:19], v[28:29], v[18:19], v[22:23]
	v_lshrrev_b32_e32 v16, 16, v16
	v_add3_u32 v17, v17, v20, s22
	v_pk_fma_f32 v[10:11], v[10:11], v[14:15], v[26:27]
	v_lshrrev_b32_e32 v8, 16, v8
	v_add3_u32 v9, v9, v12, s22
	v_and_or_b32 v16, v17, s23, v16
	v_bfe_u32 v17, v18, 16, 1
	v_and_or_b32 v8, v9, s23, v8
	v_bfe_u32 v9, v10, 16, 1
	v_add3_u32 v17, v18, v17, s22
	v_bfe_u32 v18, v19, 16, 1
	v_add3_u32 v9, v10, v9, s22
	v_bfe_u32 v10, v11, 16, 1
	v_lshrrev_b32_e32 v17, 16, v17
	v_add3_u32 v18, v19, v18, s22
	v_lshrrev_b32_e32 v9, 16, v9
	v_add3_u32 v10, v11, v10, s22
	v_and_or_b32 v17, v18, s23, v17
	v_and_or_b32 v9, v10, s23, v9
	global_store_dwordx2 v[56:57], v[16:17], off offset:2048
	global_store_dwordx2 v[56:57], v[8:9], off offset:2560
	ds_read_b128 v[8:11], v50 offset:6144
	ds_read_b128 v[12:15], v50 offset:14336
	v_pk_mul_f32 v[20:21], v[6:7], v[44:45] op_sel_hi:[1,0]
	v_pk_mul_f32 v[22:23], v[4:5], v[44:45] op_sel_hi:[1,0]
	ds_read_b128 v[4:7], v50 offset:7168
	ds_read_b128 v[16:19], v50 offset:15360
	v_pk_mul_f32 v[0:1], v[0:1], v[44:45] op_sel_hi:[1,0]
	s_waitcnt lgkmcnt(2)
	v_pk_fma_f32 v[8:9], v[22:23], v[8:9], v[12:13]
	v_pk_mul_f32 v[2:3], v[2:3], v[44:45] op_sel_hi:[1,0]
	v_bfe_u32 v12, v8, 16, 1
	s_waitcnt lgkmcnt(0)
	v_pk_fma_f32 v[0:1], v[0:1], v[4:5], v[16:17]
	v_add3_u32 v8, v8, v12, s22
	v_bfe_u32 v4, v0, 16, 1
	v_bfe_u32 v12, v9, 16, 1
	v_add3_u32 v0, v0, v4, s22
	v_bfe_u32 v4, v1, 16, 1
	v_pk_fma_f32 v[10:11], v[20:21], v[10:11], v[14:15]
	v_lshrrev_b32_e32 v8, 16, v8
	v_add3_u32 v9, v9, v12, s22
	v_pk_fma_f32 v[2:3], v[2:3], v[6:7], v[18:19]
	v_lshrrev_b32_e32 v0, 16, v0
	v_add3_u32 v1, v1, v4, s22
	v_and_or_b32 v8, v9, s23, v8
	v_bfe_u32 v9, v10, 16, 1
	v_and_or_b32 v0, v1, s23, v0
	v_bfe_u32 v1, v2, 16, 1
	v_add3_u32 v9, v10, v9, s22
	v_bfe_u32 v10, v11, 16, 1
	v_add3_u32 v1, v2, v1, s22
	v_bfe_u32 v2, v3, 16, 1
	v_lshrrev_b32_e32 v9, 16, v9
	v_add3_u32 v10, v11, v10, s22
	v_lshrrev_b32_e32 v1, 16, v1
	v_add3_u32 v2, v3, v2, s22
	v_and_or_b32 v9, v10, s23, v9
	v_and_or_b32 v1, v2, s23, v1
	v_add_co_u32_e32 v52, vcc, s28, v42
	global_store_dwordx2 v[56:57], v[8:9], off offset:3072
	global_store_dwordx2 v[56:57], v[0:1], off offset:3584
	v_addc_co_u32_e32 v53, vcc, 0, v43, vcc
	global_load_dwordx4 v[28:31], v[52:53], off offset:-4096
	v_add_co_u32_e32 v42, vcc, s25, v42
	s_nop 1
	v_addc_co_u32_e32 v43, vcc, 0, v43, vcc
	global_load_dwordx4 v[24:27], v[42:43], off offset:1024
	global_load_dwordx4 v[20:23], v[42:43], off offset:2048
	global_load_dwordx4 v[16:19], v[42:43], off offset:3072
	global_load_dwordx4 v[12:15], v[52:53], off
	global_load_dwordx4 v[8:11], v[52:53], off offset:1024
	global_load_dwordx4 v[4:7], v[52:53], off offset:2048
	global_load_dwordx4 v[0:3], v[52:53], off offset:3072
	s_waitcnt vmcnt(7)
; __device__ __forceinline__ float dot4(f32x4 a, f32x4 b) { return (a.x * b.x + a.y * b.y) + (a.z * b.z + a.w * b.w); }
; __device__ __forceinline__ float wave_sum(float v) {
; #pragma unroll
;     for (int o = 1; o < 64; o <<= 1) v += __shfl_xor(v, o);
;     return v;
; }
; __device__ __forceinline__ void phase8(KP kp, LAS unsigned char* lds, int wave, int bid) {
;     ...
;         for (int j = 0; j < 8; ++j) { v[j] = xr[64 * j]; s += dot4(v[j], v[j]); }
;         const float rstd = 1.0f / sqrtf(wave_sum(s) * (1.0f / DM) + EPS);
;         if (lane == 0) rs[lt] = rstd;
	v_mul_f32_e32 v42, v29, v29
	v_mul_f32_e32 v43, v31, v31
	v_fmac_f32_e32 v42, v28, v28
	v_fmac_f32_e32 v43, v30, v30
	v_add_f32_e32 v42, v42, v43
	s_waitcnt vmcnt(6)
	v_mul_f32_e32 v43, v25, v25
	v_mul_f32_e32 v44, v27, v27
	v_fmac_f32_e32 v43, v24, v24
	v_fmac_f32_e32 v44, v26, v26
	v_add_f32_e32 v43, v43, v44
	v_add_f32_e32 v42, v42, v43
	s_waitcnt vmcnt(5)
	v_mul_f32_e32 v43, v21, v21
	v_mul_f32_e32 v44, v23, v23
	v_fmac_f32_e32 v43, v20, v20
	v_fmac_f32_e32 v44, v22, v22
	v_add_f32_e32 v43, v43, v44
	v_add_f32_e32 v42, v42, v43
	s_waitcnt vmcnt(4)
	v_mul_f32_e32 v43, v17, v17
	v_mul_f32_e32 v44, v19, v19
	v_fmac_f32_e32 v43, v16, v16
	v_fmac_f32_e32 v44, v18, v18
	v_add_f32_e32 v43, v43, v44
	v_add_f32_e32 v42, v42, v43
	s_waitcnt vmcnt(3)
	v_mul_f32_e32 v43, v13, v13
	v_mul_f32_e32 v44, v15, v15
	v_fmac_f32_e32 v43, v12, v12
	v_fmac_f32_e32 v44, v14, v14
	v_add_f32_e32 v43, v43, v44
	v_add_f32_e32 v42, v42, v43
	s_waitcnt vmcnt(2)
	v_mul_f32_e32 v43, v9, v9
	v_mul_f32_e32 v44, v11, v11
	v_fmac_f32_e32 v43, v8, v8
	v_fmac_f32_e32 v44, v10, v10
	v_add_f32_e32 v43, v43, v44
	v_add_f32_e32 v42, v42, v43
	s_waitcnt vmcnt(1)
	v_mul_f32_e32 v43, v5, v5
	v_mul_f32_e32 v44, v7, v7
	v_fmac_f32_e32 v43, v4, v4
	v_fmac_f32_e32 v44, v6, v6
	v_add_f32_e32 v43, v43, v44
	v_add_f32_e32 v42, v42, v43
	s_waitcnt vmcnt(0)
	v_mul_f32_e32 v43, v1, v1
	v_mul_f32_e32 v44, v3, v3
	v_fmac_f32_e32 v43, v0, v0
	v_fmac_f32_e32 v44, v2, v2
	v_add_f32_e32 v43, v43, v44
	v_add_f32_e32 v42, v42, v43
	s_nop 1
	v_add_f32_dpp v42, v42, v42 quad_perm:[1,0,3,2] row_mask:0xf bank_mask:0xf
	s_nop 1
	v_add_f32_dpp v42, v42, v42 quad_perm:[2,3,0,1] row_mask:0xf bank_mask:0xf
	s_nop 1
	v_add_f32_dpp v42, v42, v42 row_half_mirror row_mask:0xf bank_mask:0xf
	s_nop 1
	v_add_f32_dpp v42, v42, v42 row_mirror row_mask:0xf bank_mask:0xf
	v_mov_b32_e32 v43, v42
	s_nop 1
	v_permlane16_swap_b32_e32 v42, v43
	v_add_f32_e32 v42, v42, v43
	v_mov_b32_e32 v43, v42
	s_nop 1
	v_permlane32_swap_b32_e32 v42, v43
	v_add_f32_e32 v42, v42, v43
	v_fmamk_f32 v42, v42, 0x3a000000, v35
	v_mul_f32_e32 v43, 0x4f800000, v42
	v_cmp_gt_f32_e32 vcc, s21, v42
	s_nop 1
	v_cndmask_b32_e32 v42, v42, v43, vcc
	v_sqrt_f32_e32 v43, v42
	s_nop 0
	v_add_u32_e32 v44, -1, v43
	v_fma_f32 v52, -v44, v43, v42
	v_cmp_ge_f32_e64 s[6:7], 0, v52
	v_add_u32_e32 v52, 1, v43
	s_nop 0
	v_cndmask_b32_e64 v44, v43, v44, s[6:7]
	v_fma_f32 v43, -v52, v43, v42
	v_cmp_lt_f32_e64 s[6:7], 0, v43
	s_nop 1
	v_cndmask_b32_e64 v43, v44, v52, s[6:7]
	v_mul_f32_e32 v44, 0x37800000, v43
	v_cndmask_b32_e32 v43, v43, v44, vcc
	v_cmp_class_f32_e32 vcc, v42, v51
	s_nop 1
	v_cndmask_b32_e32 v42, v43, v42, vcc
	v_div_scale_f32 v43, s[6:7], v42, v42, 1.0
	v_rcp_f32_e32 v44, v43
	s_nop 0
	v_fma_f32 v52, -v43, v44, 1.0
	v_fmac_f32_e32 v44, v52, v44
	v_div_scale_f32 v52, vcc, 1.0, v42, 1.0
	v_mul_f32_e32 v53, v52, v44
	v_fma_f32 v54, -v43, v53, v52
	v_fmac_f32_e32 v53, v54, v44
	v_fma_f32 v43, -v43, v53, v52
	v_div_fmas_f32 v43, v43, v44, v53
	v_div_fixup_f32 v42, v43, v42, 1.0
	s_and_saveexec_b64 s[6:7], s[2:3]
	s_cbranch_execz .LBB0_932
	s_add_i32 s4, s5, s18
	v_mov_b32_e32 v43, s4
	ds_write_b32 v43, v42 offset:4
	s_branch .LBB0_932

; #define GAS __attribute__((address_space(1)))
; __device__ __forceinline__ f32x4 unpack4(u32x2 w) { return (f32x4){bflo(w.x), bfhi(w.x), bflo(w.y), bfhi(w.y)}; }
; __device__ __forceinline__ void phase12(KP kp, LAS unsigned char* lds, int wave, int bid, int G) {
;     ...
;     for (int m = bid * NWAVES + wave; m < T; m += G * NWAVES) {
;         const GAS f32x4* xr = (const GAS f32x4*)(X1 + (size_t)m * DM) + lane;
;         const i32x4 te = *(const GAS i32x4*)(TOPI + m * 4), rk = *(const GAS i32x4*)(TRANK + m * 4); const f32x4 tw = *(const GAS f32x4*)(TOPW + m * 4);
;         const i32x4 sl = (i32x4){pstart[te.x] + rk.x, pstart[te.y] + rk.y, pstart[te.z] + rk.z, pstart[te.w] + rk.w};
;         const GAS u32x2* y0 = (const GAS u32x2*)(YS + (size_t)sl.x * DM) + lane; const GAS u32x2* y1 = (const GAS u32x2*)(YS + (size_t)sl.y * DM) + lane;
;         const GAS u32x2* y2 = (const GAS u32x2*)(YS + (size_t)sl.z * DM) + lane; const GAS u32x2* y3 = (const GAS u32x2*)(YS + (size_t)sl.w * DM) + lane;
;         f32x4 v[8]; float s = 0.f;
; #pragma unroll
;         for (int j = 0; j < 8; ++j) {
;             const f32x4 mo = tw.x * unpack4(y0[64 * j]) + tw.y * unpack4(y1[64 * j]) + tw.z * unpack4(y2[64 * j]) + tw.w * unpack4(y3[64 * j]);
.LBB0_4682:
	v_lshl_add_u64 v[36:37], s[12:13], 0, v[90:91]
	s_ashr_i32 s5, s4, 31
	v_add_co_u32_e32 v104, vcc, s7, v36
	s_lshl_b64 s[0:1], s[4:5], 2
	s_nop 0
	v_addc_co_u32_e32 v105, vcc, 0, v37, vcc
	v_add_co_u32_e32 v106, vcc, s21, v36
	s_add_u32 s24, s14, s0
	s_nop 0
	v_addc_co_u32_e32 v107, vcc, 0, v37, vcc
	s_addc_u32 s25, s15, s1
	global_load_dwordx4 v[0:3], v[70:71], off
	global_load_dwordx4 v[4:7], v[70:71], off offset:1024
	global_load_dwordx4 v[8:11], v[70:71], off offset:2048
	global_load_dwordx4 v[12:15], v[70:71], off offset:3072
	global_load_dwordx4 v[16:19], v[74:75], off
	global_load_dwordx4 v[20:23], v[76:77], off
	global_load_dwordx4 v[24:27], v[78:79], off
	global_load_dwordx4 v[32:35], v[80:81], off
	global_load_dwordx4 v[28:31], v[72:73], off
	global_load_dwordx4 v[60:63], v[104:105], off offset:1024
	global_load_dwordx4 v[56:59], v[104:105], off offset:2048
	global_load_dwordx4 v[48:51], v[104:105], off offset:3072
	global_load_dwordx4 v[64:67], v[106:107], off offset:-4096
	global_load_dwordx4 v[52:55], v[106:107], off
	global_load_dwordx4 v[44:47], v[106:107], off offset:1024
	global_load_dwordx4 v[40:43], v[106:107], off offset:2048
	global_load_dwordx4 v[36:39], v[106:107], off offset:3072
	v_lshl_add_u64 v[92:93], s[8:9], 0, v[90:91]
	global_load_dwordx4 v[104:107], v100, s[24:25]
	s_add_u32 s24, s17, s0
	s_addc_u32 s25, s18, s1
	global_load_dwordx4 v[108:111], v100, s[24:25]
	s_add_u32 s0, s19, s0
	s_addc_u32 s1, s20, s1
	global_load_dwordx4 v[112:115], v100, s[0:1]
	s_add_i32 s2, s2, s6
	s_add_i32 s4, s4, s16
	s_add_u32 s8, s8, s10
	s_addc_u32 s9, s9, s11
	s_add_u32 s12, s12, s10
	s_addc_u32 s13, s13, s11
	s_cmpk_lt_i32 s2, 0x2000
	s_waitcnt vmcnt(2)
	v_lshlrev_b32_e32 v103, 2, v104
	v_lshlrev_b32_e32 v104, 2, v105
	v_lshlrev_b32_e32 v105, 2, v106
	v_lshlrev_b32_e32 v106, 2, v107
	v_add_u32_e32 v103, s3, v103
	v_add_u32_e32 v105, s3, v105
	v_add_u32_e32 v104, s3, v104
	v_add_u32_e32 v106, s3, v106
	ds_read_b32 v103, v103
	ds_read_b32 v107, v104
	ds_read_b32 v105, v105
	ds_read_b32 v116, v106
	s_waitcnt vmcnt(0)
	v_mov_b32_e32 v104, v115
	s_waitcnt lgkmcnt(3)
	v_add_u32_e32 v106, v103, v108
	s_waitcnt lgkmcnt(2)
	v_add_u32_e32 v108, v107, v109
	s_waitcnt lgkmcnt(1)
	v_add_u32_e32 v110, v105, v110
	s_waitcnt lgkmcnt(0)
	v_add_u32_e32 v116, v116, v111
	v_ashrrev_i32_e32 v107, 31, v106
	v_ashrrev_i32_e32 v109, 31, v108
	v_ashrrev_i32_e32 v111, 31, v110
	v_ashrrev_i32_e32 v117, 31, v116
	v_lshlrev_b64 v[106:107], 12, v[106:107]
	v_lshlrev_b64 v[108:109], 12, v[108:109]
	v_lshlrev_b64 v[110:111], 12, v[110:111]
	v_lshlrev_b64 v[116:117], 12, v[116:117]
	v_lshl_add_u64 v[106:107], v[68:69], 0, v[106:107]
	v_lshl_add_u64 v[108:109], v[68:69], 0, v[108:109]
	v_lshl_add_u64 v[110:111], v[68:69], 0, v[110:111]
	v_lshl_add_u64 v[116:117], v[68:69], 0, v[116:117]
	global_load_dwordx2 v[118:119], v[106:107], off
	global_load_dwordx2 v[120:121], v[108:109], off
	global_load_dwordx2 v[122:123], v[110:111], off
	global_load_dwordx2 v[124:125], v[116:117], off
	global_load_dwordx2 v[126:127], v[106:107], off offset:512
	global_load_dwordx2 v[128:129], v[108:109], off offset:512
	global_load_dwordx2 v[130:131], v[110:111], off offset:512
	global_load_dwordx2 v[132:133], v[116:117], off offset:512
	global_load_dwordx2 v[134:135], v[106:107], off offset:1024
	global_load_dwordx2 v[136:137], v[108:109], off offset:1024
	global_load_dwordx2 v[138:139], v[110:111], off offset:1024
	global_load_dwordx2 v[140:141], v[116:117], off offset:1024
	global_load_dwordx2 v[142:143], v[106:107], off offset:1536
	global_load_dwordx2 v[144:145], v[108:109], off offset:1536
	global_load_dwordx2 v[146:147], v[110:111], off offset:1536
	global_load_dwordx2 v[148:149], v[116:117], off offset:1536
	global_load_dwordx2 v[150:151], v[106:107], off offset:2048
	global_load_dwordx2 v[152:153], v[106:107], off offset:2560
	global_load_dwordx2 v[154:155], v[106:107], off offset:3072
	s_nop 0
	global_load_dwordx2 v[106:107], v[106:107], off offset:3584
	s_nop 0
	global_load_dwordx2 v[156:157], v[108:109], off offset:2048
	global_load_dwordx2 v[158:159], v[108:109], off offset:2560
	global_load_dwordx2 v[160:161], v[108:109], off offset:3072
	s_nop 0
	global_load_dwordx2 v[108:109], v[108:109], off offset:3584
	s_nop 0
	global_load_dwordx2 v[162:163], v[110:111], off offset:2048
	global_load_dwordx2 v[164:165], v[110:111], off offset:2560
	global_load_dwordx2 v[166:167], v[110:111], off offset:3072
	s_nop 0
	global_load_dwordx2 v[110:111], v[110:111], off offset:3584
	s_nop 0
	global_load_dwordx2 v[168:169], v[116:117], off offset:2048
	global_load_dwordx2 v[170:171], v[116:117], off offset:2560
	global_load_dwordx2 v[172:173], v[116:117], off offset:3072
	s_nop 0
	global_load_dwordx2 v[116:117], v[116:117], off offset:3584
	s_waitcnt vmcnt(31)
	v_lshlrev_b32_e32 v174, 16, v118
	s_waitcnt vmcnt(30)
	v_lshlrev_b32_e32 v176, 16, v120
	v_and_b32_e32 v177, 0xffff0000, v120
	v_lshlrev_b32_e32 v120, 16, v121
	v_and_b32_e32 v121, 0xffff0000, v121
	s_waitcnt vmcnt(26)
	v_lshlrev_b32_e32 v184, 16, v128
	v_and_b32_e32 v185, 0xffff0000, v128
	v_lshlrev_b32_e32 v128, 16, v129
	v_and_b32_e32 v129, 0xffff0000, v129
	v_and_b32_e32 v175, 0xffff0000, v118
	v_lshlrev_b32_e32 v118, 16, v119
	v_and_b32_e32 v119, 0xffff0000, v119
	v_lshlrev_b32_e32 v182, 16, v126
	v_and_b32_e32 v183, 0xffff0000, v126
	v_lshlrev_b32_e32 v126, 16, v127
	v_and_b32_e32 v127, 0xffff0000, v127
	s_waitcnt vmcnt(22)
	v_lshlrev_b32_e32 v192, 16, v136
	v_and_b32_e32 v193, 0xffff0000, v136
	v_lshlrev_b32_e32 v136, 16, v137
	v_and_b32_e32 v137, 0xffff0000, v137
	s_waitcnt vmcnt(18)
; __device__ __forceinline__ float bflo(unsigned w) { return __uint_as_float(w << 16); }
; __device__ __forceinline__ float bfhi(unsigned w) { return __uint_as_float(w & 0xffff0000u); }
; __device__ __forceinline__ f32x4 unpack4(u32x2 w) { return (f32x4){bflo(w.x), bfhi(w.x), bflo(w.y), bfhi(w.y)}; }
; __device__ __forceinline__ void phase12(KP kp, LAS unsigned char* lds, int wave, int bid, int G) {
;     ...
;         for (int j = 0; j < 8; ++j) {
;             const f32x4 mo = tw.x * unpack4(y0[64 * j]) + tw.y * unpack4(y1[64 * j]) + tw.z * unpack4(y2[64 * j]) + tw.w * unpack4(y3[64 * j]);
	v_lshlrev_b32_e32 v200, 16, v144
	v_and_b32_e32 v201, 0xffff0000, v144
	v_lshlrev_b32_e32 v144, 16, v145
	v_and_b32_e32 v145, 0xffff0000, v145
	s_waitcnt vmcnt(11)
	v_lshlrev_b32_e32 v208, 16, v156
	v_and_b32_e32 v209, 0xffff0000, v156
	v_lshlrev_b32_e32 v156, 16, v157
	v_and_b32_e32 v157, 0xffff0000, v157
	s_waitcnt vmcnt(10)
	v_lshlrev_b32_e32 v216, 16, v158
	v_and_b32_e32 v217, 0xffff0000, v158
	v_lshlrev_b32_e32 v158, 16, v159
	v_and_b32_e32 v159, 0xffff0000, v159
	s_waitcnt vmcnt(9)
	v_lshlrev_b32_e32 v224, 16, v160
	v_and_b32_e32 v225, 0xffff0000, v160
	v_lshlrev_b32_e32 v160, 16, v161
	v_and_b32_e32 v161, 0xffff0000, v161
	s_waitcnt vmcnt(8)
	v_lshlrev_b32_e32 v232, 16, v108
	v_and_b32_e32 v233, 0xffff0000, v108
	v_lshlrev_b32_e32 v108, 16, v109
	v_and_b32_e32 v109, 0xffff0000, v109
	v_pk_mul_f32 v[120:121], v[112:113], v[120:121] op_sel:[1,0]
	v_pk_mul_f32 v[176:177], v[112:113], v[176:177] op_sel:[1,0]
	v_pk_mul_f32 v[128:129], v[112:113], v[128:129] op_sel:[1,0]
	v_pk_mul_f32 v[184:185], v[112:113], v[184:185] op_sel:[1,0]
	v_lshlrev_b32_e32 v178, 16, v122
	v_and_b32_e32 v179, 0xffff0000, v122
	v_lshlrev_b32_e32 v122, 16, v123
	v_and_b32_e32 v123, 0xffff0000, v123
	v_lshlrev_b32_e32 v186, 16, v130
	v_and_b32_e32 v187, 0xffff0000, v130
	v_lshlrev_b32_e32 v130, 16, v131
	v_and_b32_e32 v131, 0xffff0000, v131
	v_lshlrev_b32_e32 v190, 16, v134
	v_and_b32_e32 v191, 0xffff0000, v134
	v_lshlrev_b32_e32 v134, 16, v135
	v_and_b32_e32 v135, 0xffff0000, v135
	v_lshlrev_b32_e32 v198, 16, v142
	v_and_b32_e32 v199, 0xffff0000, v142
	v_lshlrev_b32_e32 v142, 16, v143
	v_and_b32_e32 v143, 0xffff0000, v143
	v_lshlrev_b32_e32 v206, 16, v150
	v_and_b32_e32 v207, 0xffff0000, v150
	v_lshlrev_b32_e32 v150, 16, v151
	v_and_b32_e32 v151, 0xffff0000, v151
	v_lshlrev_b32_e32 v214, 16, v152
	v_and_b32_e32 v215, 0xffff0000, v152
	v_lshlrev_b32_e32 v152, 16, v153
	v_and_b32_e32 v153, 0xffff0000, v153
	v_lshlrev_b32_e32 v222, 16, v154
	v_and_b32_e32 v223, 0xffff0000, v154
	v_lshlrev_b32_e32 v154, 16, v155
	v_and_b32_e32 v155, 0xffff0000, v155
	v_lshlrev_b32_e32 v230, 16, v106
	v_and_b32_e32 v231, 0xffff0000, v106
	v_lshlrev_b32_e32 v106, 16, v107
	v_and_b32_e32 v107, 0xffff0000, v107
	v_pk_mul_f32 v[192:193], v[112:113], v[192:193] op_sel:[1,0]
	v_pk_mul_f32 v[136:137], v[112:113], v[136:137] op_sel:[1,0]
	v_pk_mul_f32 v[144:145], v[112:113], v[144:145] op_sel:[1,0]
	v_pk_mul_f32 v[200:201], v[112:113], v[200:201] op_sel:[1,0]
	v_pk_mul_f32 v[156:157], v[112:113], v[156:157] op_sel:[1,0]
	v_pk_mul_f32 v[208:209], v[112:113], v[208:209] op_sel:[1,0]
	v_pk_mul_f32 v[216:217], v[112:113], v[216:217] op_sel:[1,0]
	v_pk_mul_f32 v[158:159], v[112:113], v[158:159] op_sel:[1,0]
	v_pk_mul_f32 v[160:161], v[112:113], v[160:161] op_sel:[1,0]
	v_pk_mul_f32 v[224:225], v[112:113], v[224:225] op_sel:[1,0]
	v_pk_mul_f32 v[108:109], v[112:113], v[108:109] op_sel:[1,0]
	v_pk_mul_f32 v[232:233], v[112:113], v[232:233] op_sel:[1,0]
	v_pk_fma_f32 v[174:175], v[112:113], v[174:175], v[176:177] op_sel_hi:[0,1,1]
	v_pk_fma_f32 v[118:119], v[112:113], v[118:119], v[120:121] op_sel_hi:[0,1,1]
	v_pk_fma_f32 v[120:121], v[112:113], v[182:183], v[184:185] op_sel_hi:[0,1,1]
	v_pk_fma_f32 v[126:127], v[112:113], v[126:127], v[128:129] op_sel_hi:[0,1,1]
	v_lshlrev_b32_e32 v180, 16, v124
	v_and_b32_e32 v181, 0xffff0000, v124
	v_lshlrev_b32_e32 v124, 16, v125
	v_and_b32_e32 v125, 0xffff0000, v125
	v_lshlrev_b32_e32 v188, 16, v132
	v_and_b32_e32 v189, 0xffff0000, v132
	v_lshlrev_b32_e32 v132, 16, v133
	v_and_b32_e32 v133, 0xffff0000, v133
	v_lshlrev_b32_e32 v194, 16, v138
	v_and_b32_e32 v195, 0xffff0000, v138
	v_lshlrev_b32_e32 v138, 16, v139
	v_and_b32_e32 v139, 0xffff0000, v139
	v_lshlrev_b32_e32 v202, 16, v146
	v_and_b32_e32 v203, 0xffff0000, v146
	v_lshlrev_b32_e32 v146, 16, v147
	v_and_b32_e32 v147, 0xffff0000, v147
	s_waitcnt vmcnt(7)
	v_lshlrev_b32_e32 v210, 16, v162
	v_and_b32_e32 v211, 0xffff0000, v162
	v_lshlrev_b32_e32 v162, 16, v163
	v_and_b32_e32 v163, 0xffff0000, v163
	s_waitcnt vmcnt(6)
	v_lshlrev_b32_e32 v218, 16, v164
	v_and_b32_e32 v219, 0xffff0000, v164
	v_lshlrev_b32_e32 v164, 16, v165
	v_and_b32_e32 v165, 0xffff0000, v165
	s_waitcnt vmcnt(5)
	v_lshlrev_b32_e32 v226, 16, v166
	v_and_b32_e32 v227, 0xffff0000, v166
	v_lshlrev_b32_e32 v166, 16, v167
	v_and_b32_e32 v167, 0xffff0000, v167
	s_waitcnt vmcnt(4)
	v_lshlrev_b32_e32 v234, 16, v110
	v_and_b32_e32 v235, 0xffff0000, v110
	v_lshlrev_b32_e32 v110, 16, v111
	v_and_b32_e32 v111, 0xffff0000, v111
	v_pk_fma_f32 v[128:129], v[112:113], v[134:135], v[136:137] op_sel_hi:[0,1,1]
	v_pk_fma_f32 v[134:135], v[112:113], v[190:191], v[192:193] op_sel_hi:[0,1,1]
	v_pk_fma_f32 v[136:137], v[112:113], v[198:199], v[200:201] op_sel_hi:[0,1,1]
	v_pk_fma_f32 v[142:143], v[112:113], v[142:143], v[144:145] op_sel_hi:[0,1,1]
	v_pk_fma_f32 v[144:145], v[112:113], v[206:207], v[208:209] op_sel_hi:[0,1,1]
	v_pk_fma_f32 v[150:151], v[112:113], v[150:151], v[156:157] op_sel_hi:[0,1,1]
	v_pk_fma_f32 v[152:153], v[112:113], v[152:153], v[158:159] op_sel_hi:[0,1,1]
	v_pk_fma_f32 v[156:157], v[112:113], v[214:215], v[216:217] op_sel_hi:[0,1,1]
	v_pk_fma_f32 v[158:159], v[112:113], v[222:223], v[224:225] op_sel_hi:[0,1,1]
	v_pk_fma_f32 v[154:155], v[112:113], v[154:155], v[160:161] op_sel_hi:[0,1,1]
	v_pk_fma_f32 v[160:161], v[112:113], v[230:231], v[232:233] op_sel_hi:[0,1,1]
	v_pk_fma_f32 v[106:107], v[112:113], v[106:107], v[108:109] op_sel_hi:[0,1,1]
	v_pk_fma_f32 v[108:109], v[114:115], v[122:123], v[118:119] op_sel_hi:[0,1,1]
	v_pk_fma_f32 v[112:113], v[114:115], v[178:179], v[174:175] op_sel_hi:[0,1,1]
	v_pk_fma_f32 v[118:119], v[114:115], v[130:131], v[126:127] op_sel_hi:[0,1,1]
	v_pk_fma_f32 v[120:121], v[114:115], v[186:187], v[120:121] op_sel_hi:[0,1,1]
	v_lshlrev_b32_e32 v196, 16, v140
	v_and_b32_e32 v197, 0xffff0000, v140
	v_lshlrev_b32_e32 v140, 16, v141
	v_and_b32_e32 v141, 0xffff0000, v141
	v_lshlrev_b32_e32 v204, 16, v148
	v_and_b32_e32 v205, 0xffff0000, v148
	v_lshlrev_b32_e32 v148, 16, v149
	v_and_b32_e32 v149, 0xffff0000, v149
	s_waitcnt vmcnt(3)
; #define GAS __attribute__((address_space(1)))
; __device__ __forceinline__ float dot4(f32x4 a, f32x4 b) { return (a.x * b.x + a.y * b.y) + (a.z * b.z + a.w * b.w); }
; __device__ __forceinline__ f32x4 unpack4(u32x2 w) { return (f32x4){bflo(w.x), bfhi(w.x), bflo(w.y), bfhi(w.y)}; }
; __device__ __forceinline__ void phase12(KP kp, LAS unsigned char* lds, int wave, int bid, int G) {
;     ...
;             const f32x4 mo = tw.x * unpack4(y0[64 * j]) + tw.y * unpack4(y1[64 * j]) + tw.z * unpack4(y2[64 * j]) + tw.w * unpack4(y3[64 * j]);
;             const f32x4 g2 = *(const GAS f32x4*)(mod + 5 * 2048 + 256 * j + 4 * lane);
;             v[j] = xr[64 * j] + g2 * mo; s += dot4(v[j], v[j]); }
	v_lshlrev_b32_e32 v212, 16, v168
	v_and_b32_e32 v213, 0xffff0000, v168
	v_lshlrev_b32_e32 v168, 16, v169
	v_and_b32_e32 v169, 0xffff0000, v169
	s_waitcnt vmcnt(2)
	v_lshlrev_b32_e32 v220, 16, v170
	v_and_b32_e32 v221, 0xffff0000, v170
	v_lshlrev_b32_e32 v170, 16, v171
	v_and_b32_e32 v171, 0xffff0000, v171
	s_waitcnt vmcnt(1)
	v_lshlrev_b32_e32 v228, 16, v172
	v_and_b32_e32 v229, 0xffff0000, v172
	v_lshlrev_b32_e32 v172, 16, v173
	v_and_b32_e32 v173, 0xffff0000, v173
	s_waitcnt vmcnt(0)
	v_lshlrev_b32_e32 v236, 16, v116
	v_and_b32_e32 v237, 0xffff0000, v116
	v_lshlrev_b32_e32 v116, 16, v117
	v_and_b32_e32 v117, 0xffff0000, v117
	v_pk_fma_f32 v[122:123], v[114:115], v[194:195], v[134:135] op_sel_hi:[0,1,1]
	v_pk_fma_f32 v[126:127], v[114:115], v[138:139], v[128:129] op_sel_hi:[0,1,1]
	v_pk_fma_f32 v[128:129], v[114:115], v[146:147], v[142:143] op_sel_hi:[0,1,1]
	v_pk_fma_f32 v[130:131], v[114:115], v[202:203], v[136:137] op_sel_hi:[0,1,1]
	v_pk_fma_f32 v[134:135], v[114:115], v[162:163], v[150:151] op_sel_hi:[0,1,1]
	v_pk_fma_f32 v[136:137], v[114:115], v[210:211], v[144:145] op_sel_hi:[0,1,1]
	v_pk_fma_f32 v[138:139], v[114:115], v[218:219], v[156:157] op_sel_hi:[0,1,1]
	v_pk_fma_f32 v[142:143], v[114:115], v[164:165], v[152:153] op_sel_hi:[0,1,1]
	v_pk_fma_f32 v[144:145], v[114:115], v[166:167], v[154:155] op_sel_hi:[0,1,1]
	v_pk_fma_f32 v[146:147], v[114:115], v[226:227], v[158:159] op_sel_hi:[0,1,1]
	v_pk_fma_f32 v[106:107], v[114:115], v[110:111], v[106:107] op_sel_hi:[0,1,1]
	v_pk_fma_f32 v[110:111], v[114:115], v[234:235], v[160:161] op_sel_hi:[0,1,1]
	v_pk_fma_f32 v[112:113], v[104:105], v[180:181], v[112:113] op_sel_hi:[0,1,1]
	v_pk_fma_f32 v[108:109], v[104:105], v[124:125], v[108:109] op_sel_hi:[0,1,1]
	v_pk_fma_f32 v[114:115], v[104:105], v[188:189], v[120:121] op_sel_hi:[0,1,1]
	v_pk_fma_f32 v[118:119], v[104:105], v[132:133], v[118:119] op_sel_hi:[0,1,1]
	v_pk_fma_f32 v[120:121], v[104:105], v[140:141], v[126:127] op_sel_hi:[0,1,1]
	v_pk_fma_f32 v[122:123], v[104:105], v[196:197], v[122:123] op_sel_hi:[0,1,1]
	v_pk_fma_f32 v[124:125], v[104:105], v[204:205], v[130:131] op_sel_hi:[0,1,1]
	v_pk_fma_f32 v[126:127], v[104:105], v[148:149], v[128:129] op_sel_hi:[0,1,1]
	v_pk_fma_f32 v[128:129], v[104:105], v[212:213], v[136:137] op_sel_hi:[0,1,1]
	v_pk_fma_f32 v[130:131], v[104:105], v[168:169], v[134:135] op_sel_hi:[0,1,1]
	v_pk_fma_f32 v[132:133], v[104:105], v[170:171], v[142:143] op_sel_hi:[0,1,1]
	v_pk_fma_f32 v[134:135], v[104:105], v[220:221], v[138:139] op_sel_hi:[0,1,1]
	v_pk_fma_f32 v[136:137], v[104:105], v[228:229], v[146:147] op_sel_hi:[0,1,1]
	v_pk_fma_f32 v[138:139], v[104:105], v[172:173], v[144:145] op_sel_hi:[0,1,1]
	v_pk_fma_f32 v[110:111], v[104:105], v[236:237], v[110:111] op_sel_hi:[0,1,1]
	v_pk_fma_f32 v[104:105], v[104:105], v[116:117], v[106:107] op_sel_hi:[0,1,1]
	v_pk_fma_f32 v[2:3], v[2:3], v[108:109], v[66:67]
	v_pk_fma_f32 v[0:1], v[0:1], v[112:113], v[64:65]
	v_pk_fma_f32 v[6:7], v[6:7], v[118:119], v[62:63]
	v_pk_fma_f32 v[4:5], v[4:5], v[114:115], v[60:61]
	v_pk_fma_f32 v[8:9], v[8:9], v[122:123], v[56:57]
	v_pk_fma_f32 v[10:11], v[10:11], v[120:121], v[58:59]
	v_pk_fma_f32 v[26:27], v[26:27], v[138:139], v[42:43]
	v_pk_fma_f32 v[34:35], v[34:35], v[104:105], v[38:39]
	v_mov_b32_e32 v38, v1
	v_mov_b32_e32 v39, v5
	v_mov_b32_e32 v42, v3
	v_mov_b32_e32 v43, v7
	v_pk_fma_f32 v[20:21], v[20:21], v[134:135], v[44:45]
	v_pk_fma_f32 v[22:23], v[22:23], v[132:133], v[46:47]
	v_pk_fma_f32 v[24:25], v[24:25], v[136:137], v[40:41]
	v_pk_fma_f32 v[32:33], v[32:33], v[110:111], v[36:37]
	v_mov_b32_e32 v36, v0
	v_mov_b32_e32 v37, v4
	v_mov_b32_e32 v40, v2
	v_mov_b32_e32 v41, v6
	v_pk_mul_f32 v[44:45], v[10:11], v[10:11]
	v_pk_mul_f32 v[46:47], v[8:9], v[8:9]
	v_pk_mul_f32 v[38:39], v[38:39], v[38:39]
	v_pk_mul_f32 v[42:43], v[42:43], v[42:43]
	v_pk_fma_f32 v[14:15], v[14:15], v[126:127], v[50:51]
	v_pk_fma_f32 v[12:13], v[12:13], v[124:125], v[48:49]
	v_pk_mov_b32 v[60:61], v[46:47], v[44:45] op_sel:[1,0]
	v_mov_b32_e32 v47, v45
	v_pk_fma_f32 v[36:37], v[36:37], v[36:37], v[38:39]
	v_pk_fma_f32 v[38:39], v[40:41], v[40:41], v[42:43]
	v_pk_fma_f32 v[18:19], v[18:19], v[130:131], v[54:55]
	v_pk_fma_f32 v[16:17], v[16:17], v[128:129], v[52:53]
	v_mul_f32_e32 v48, v13, v13
	v_mul_f32_e32 v50, v15, v15
	v_pk_add_f32 v[40:41], v[60:61], v[46:47]
	v_pk_add_f32 v[36:37], v[36:37], v[38:39]
	v_mul_f32_e32 v59, v16, v16
	v_mul_f32_e32 v62, v17, v17
	v_mul_f32_e32 v63, v18, v18
	v_mul_f32_e32 v64, v19, v19
	v_pk_fma_f32 v[44:45], v[12:13], v[12:13], v[48:49] op_sel_hi:[1,1,0]
	v_pk_fma_f32 v[48:49], v[14:15], v[14:15], v[50:51] op_sel_hi:[1,1,0]
	v_pk_add_f32 v[38:39], v[40:41], v[40:41] op_sel:[0,1] op_sel_hi:[1,0]
	v_pk_add_f32 v[36:37], v[36:37], v[36:37] op_sel:[0,1] op_sel_hi:[1,0]
	v_pk_mul_f32 v[52:53], v[22:23], v[22:23]
	v_pk_mul_f32 v[54:55], v[20:21], v[20:21]
	v_mov_b32_e32 v45, v63
	v_mov_b32_e32 v49, v64
	v_mov_b32_e32 v39, v62
	v_mov_b32_e32 v37, v59
; #define GAS __attribute__((address_space(1)))
; __device__ __forceinline__ float dot4(f32x4 a, f32x4 b) { return (a.x * b.x + a.y * b.y) + (a.z * b.z + a.w * b.w); }
; __device__ __forceinline__ float wave_sum(float v) {
; #pragma unroll
;     for (int o = 1; o < 64; o <<= 1) v += __shfl_xor(v, o);
;     return v;
; }
; __device__ __forceinline__ void phase12(KP kp, LAS unsigned char* lds, int wave, int bid, int G) {
;     ...
;             v[j] = xr[64 * j] + g2 * mo; s += dot4(v[j], v[j]); }
;         const float rstd = 1.0f / sqrtf(wave_sum(s) * (1.0f / DM) + EPS);
;         GAS f32x4* o = (GAS f32x4*)(KOUT() + (size_t)m * DM) + lane;
; #pragma unroll
;         for (int j = 0; j < 8; ++j) o[64 * j] = v[j] * rstd * *(const GAS f32x4*)(fg + 256 * j + 4 * lane);
	v_pk_mov_b32 v[50:51], v[54:55], v[52:53] op_sel:[1,0]
	v_mov_b32_e32 v55, v53
	v_pk_add_f32 v[40:41], v[44:45], v[48:49]
	v_pk_add_f32 v[36:37], v[36:37], v[38:39]
	v_mul_f32_e32 v56, v25, v25
	v_mul_f32_e32 v58, v27, v27
	v_pk_add_f32 v[42:43], v[50:51], v[54:55]
	v_pk_add_f32 v[36:37], v[36:37], v[40:41]
	v_mul_f32_e32 v65, v32, v32
	v_mul_f32_e32 v66, v33, v33
	v_mul_f32_e32 v67, v34, v34
	v_mul_f32_e32 v103, v35, v35
	v_pk_fma_f32 v[52:53], v[24:25], v[24:25], v[56:57] op_sel_hi:[1,1,0]
	v_pk_fma_f32 v[56:57], v[26:27], v[26:27], v[58:59] op_sel_hi:[1,1,0]
	v_pk_add_f32 v[42:43], v[42:43], v[42:43] op_sel:[0,1] op_sel_hi:[1,0]
	v_pk_add_f32 v[36:37], v[36:37], v[36:37] op_sel:[0,1] op_sel_hi:[1,0]
	v_mov_b32_e32 v53, v67
	v_mov_b32_e32 v57, v103
	v_mov_b32_e32 v43, v66
	v_mov_b32_e32 v37, v65
	v_pk_add_f32 v[44:45], v[52:53], v[56:57]
	v_pk_add_f32 v[36:37], v[36:37], v[42:43]
	s_nop 0
	v_pk_add_f32 v[36:37], v[36:37], v[44:45]
	s_nop 0
	v_add_f32_e32 v36, v36, v37
	s_nop 1
	v_add_f32_dpp v36, v36, v36 quad_perm:[1,0,3,2] row_mask:0xf bank_mask:0xf
	s_nop 1
	v_add_f32_dpp v36, v36, v36 quad_perm:[2,3,0,1] row_mask:0xf bank_mask:0xf
	s_nop 1
	v_add_f32_dpp v36, v36, v36 row_half_mirror row_mask:0xf bank_mask:0xf
	s_nop 1
	v_add_f32_dpp v36, v36, v36 row_mirror row_mask:0xf bank_mask:0xf
	v_mov_b32_e32 v37, v36
	s_nop 1
	v_permlane16_swap_b32_e32 v36, v37
	v_add_f32_e32 v36, v36, v37
	v_mov_b32_e32 v37, v36
	s_nop 1
	v_permlane32_swap_b32_e32 v36, v37
	v_add_f32_e32 v36, v36, v37
	v_fmamk_f32 v36, v36, 0x3a000000, v101
	v_mul_f32_e32 v37, 0x4f800000, v36
	v_cmp_gt_f32_e32 vcc, s22, v36
	s_nop 1
	v_cndmask_b32_e32 v36, v36, v37, vcc
	v_sqrt_f32_e32 v37, v36
	s_nop 0
	v_add_u32_e32 v38, -1, v37
	v_add_u32_e32 v39, 1, v37
	v_fma_f32 v40, -v38, v37, v36
	v_fma_f32 v41, -v39, v37, v36
	v_cmp_ge_f32_e64 s[0:1], 0, v40
	s_nop 1
	v_cndmask_b32_e64 v37, v37, v38, s[0:1]
	v_cmp_lt_f32_e64 s[0:1], 0, v41
	s_nop 1
	v_cndmask_b32_e64 v37, v37, v39, s[0:1]
	v_mul_f32_e32 v38, 0x37800000, v37
	v_cndmask_b32_e32 v37, v37, v38, vcc
	v_cmp_class_f32_e32 vcc, v36, v102
	s_nop 1
	v_cndmask_b32_e32 v36, v37, v36, vcc
	v_div_scale_f32 v37, s[0:1], v36, v36, 1.0
	v_rcp_f32_e32 v39, v37
	v_div_scale_f32 v38, vcc, 1.0, v36, 1.0
	v_fma_f32 v40, -v37, v39, 1.0
	v_fmac_f32_e32 v39, v40, v39
	v_mul_f32_e32 v40, v38, v39
	v_fma_f32 v41, -v37, v40, v38
	v_fmac_f32_e32 v40, v41, v39
	v_fma_f32 v37, -v37, v40, v38
	v_div_fmas_f32 v37, v37, v39, v40
	v_div_fixup_f32 v36, v37, v36, 1.0
	v_pk_mul_f32 v[0:1], v[0:1], v[36:37] op_sel_hi:[1,0]
	v_pk_mul_f32 v[2:3], v[2:3], v[36:37] op_sel_hi:[1,0]
	v_pk_mul_f32 v[0:1], v[28:29], v[0:1]
	v_pk_mul_f32 v[2:3], v[30:31], v[2:3]
	global_store_dwordx4 v[92:93], v[0:3], off
	global_load_dwordx4 v[0:3], v[72:73], off offset:1024
	v_pk_mul_f32 v[6:7], v[6:7], v[36:37] op_sel_hi:[1,0]
	v_pk_mul_f32 v[4:5], v[4:5], v[36:37] op_sel_hi:[1,0]
	s_waitcnt vmcnt(0)
	v_pk_mul_f32 v[2:3], v[2:3], v[6:7]
	v_pk_mul_f32 v[0:1], v[0:1], v[4:5]
	global_store_dwordx4 v[92:93], v[0:3], off offset:1024
	global_load_dwordx4 v[0:3], v[72:73], off offset:2048
	v_pk_mul_f32 v[4:5], v[10:11], v[36:37] op_sel_hi:[1,0]
	v_pk_mul_f32 v[6:7], v[8:9], v[36:37] op_sel_hi:[1,0]
	v_pk_mul_f32 v[8:9], v[16:17], v[36:37] op_sel_hi:[1,0]
	s_waitcnt vmcnt(0)
	v_pk_mul_f32 v[0:1], v[0:1], v[6:7]
	v_pk_mul_f32 v[2:3], v[2:3], v[4:5]
	global_store_dwordx4 v[92:93], v[0:3], off offset:2048
	global_load_dwordx4 v[0:3], v[72:73], off offset:3072
	v_pk_mul_f32 v[4:5], v[14:15], v[36:37] op_sel_hi:[1,0]
	v_pk_mul_f32 v[6:7], v[12:13], v[36:37] op_sel_hi:[1,0]
	s_waitcnt vmcnt(0)
	v_pk_mul_f32 v[2:3], v[2:3], v[4:5]
	v_pk_mul_f32 v[0:1], v[0:1], v[6:7]
	global_store_dwordx4 v[92:93], v[0:3], off offset:3072
	global_load_dwordx4 v[0:3], v[82:83], off
	v_add_co_u32_e32 v4, vcc, s23, v92
	v_pk_mul_f32 v[6:7], v[18:19], v[36:37] op_sel_hi:[1,0]
	s_nop 0
	v_addc_co_u32_e32 v5, vcc, 0, v93, vcc
	s_waitcnt vmcnt(0)
	v_pk_mul_f32 v[0:1], v[0:1], v[8:9]
	v_pk_mul_f32 v[2:3], v[2:3], v[6:7]
	global_store_dwordx4 v[4:5], v[0:3], off
	global_load_dwordx4 v[0:3], v[84:85], off
	v_pk_mul_f32 v[6:7], v[22:23], v[36:37] op_sel_hi:[1,0]
	v_pk_mul_f32 v[8:9], v[20:21], v[36:37] op_sel_hi:[1,0]
	s_waitcnt vmcnt(0)
	v_pk_mul_f32 v[2:3], v[2:3], v[6:7]
	v_pk_mul_f32 v[0:1], v[0:1], v[8:9]
	global_store_dwordx4 v[4:5], v[0:3], off offset:1024
	global_load_dwordx4 v[0:3], v[86:87], off
	v_pk_mul_f32 v[6:7], v[26:27], v[36:37] op_sel_hi:[1,0]
	v_pk_mul_f32 v[8:9], v[24:25], v[36:37] op_sel_hi:[1,0]
	s_waitcnt vmcnt(0)
	v_pk_mul_f32 v[2:3], v[2:3], v[6:7]
	v_pk_mul_f32 v[0:1], v[0:1], v[8:9]
	global_store_dwordx4 v[4:5], v[0:3], off offset:2048
	global_load_dwordx4 v[0:3], v[88:89], off
	v_pk_mul_f32 v[6:7], v[34:35], v[36:37] op_sel_hi:[1,0]
	v_pk_mul_f32 v[8:9], v[32:33], v[36:37] op_sel_hi:[1,0]
	s_waitcnt vmcnt(0)
	v_pk_mul_f32 v[2:3], v[2:3], v[6:7]
	v_pk_mul_f32 v[0:1], v[0:1], v[8:9]
	global_store_dwordx4 v[4:5], v[0:3], off offset:3072
	s_cbranch_scc1 .LBB0_4682
